# v47 + P4 LN1 weight/bias fragments loaded once per wave (row loop had 8 dependent round trips per row) + ret_out state image: 8 loads requested together
# speedup vs baseline: 1.0019x; 1.0019x over previous
; DI int lane_id() { int l; asm volatile("v_mbcnt_lo_u32_b32 %0, -1, 0\n\tv_mbcnt_hi_u32_b32 %0, -1, %0" : "=v"(l)); return l; }
; DI KPtr kargs() { KPtr p = (KPtr)__builtin_amdgcn_kernarg_segment_ptr(); asm volatile("" : "+s"(p)); return p; }
; DI float head_log_gamma(int h) { return log1pf(-exp2f(-5.0f - (float)h)); }
; template <bool TRIMG>
; DI void stage_rope(const Ctx& c, unsigned dst, int stride, int t0, int col0, int pos0, float scale, float lg, bool kdec) {
;     const u16* proj = (const u16*)(c.ws + WS_PROJ); const f32x2* rope = (const f32x2*)(c.ws + WS_ROPE); const int tid = c.wid * 64 + lane_id();
; #pragma unroll
;     for (int it = 0; it < 2; ++it) { const int item = tid + it * NTHR, j = item >> 3, pc = item & 7, dd = pc * 8;
;         const u16* rp = proj + (size_t)(t0 + j) * INC + col0 + dd;
;         const u32x4 a = *(const u32x4*)rp, b = *(const u32x4*)(rp + 64);
;         const f32x4* cs = (const f32x4*)(rope + (size_t)(pos0 + j) * 64 + dd);
;         const f32x4 c0 = cs[0], c1 = cs[1], c2 = cs[2], c3 = cs[3];
;         const float sc = kdec ? scale * __expf((float)(127 - j) * lg) : scale;
; DI void ret_out_unit(const Ctx& c, int u) {
;     const KPtr kp = kargs();
;     const int h = u & 7, n = (u >> 3) & 15, b = u >> 7;
;     const int t0 = b * SEQ + n * CHUNK; const float lg = head_log_gamma(h);
;     const unsigned base = (unsigned)(size_t)c.lds, Qimg = base, Kimg = base + IMG_R, Vimg = base + 2 * IMG_R, Simg = base + 2 * IMG_R + IMG_T;
;     const u16* proj = (const u16*)(c.ws + WS_PROJ);
;     __syncthreads();
;     u32x2 gbv[8]; f32x4 gwv[8];
;     { const int l0 = lane_id(), il0 = 16 * c.wid + (l0 & 15), fq0 = l0 >> 4; const float* gnw0 = kp->in[3] + h * 128;
; #pragma unroll
;       for (int ef = 0; ef < 8; ++ef) { const int e = ef * 16 + 4 * fq0; gwv[ef] = *(const f32x4*)(gnw0 + e); gbv[ef] = *(const u32x2*)(proj + (size_t)(t0 + il0) * INC + 3 * RW + h * 128 + e); } }
;     stage_rope<false>(c, Qimg, RS, t0, h * 128, n * CHUNK, 1.0f, lg, false);
;     stage_rope<false>(c, Kimg, RS, t0, RW + h * 128, n * CHUNK, 0.08838834764831845f, lg, false);
.LBB0_273:
	s_bitcmp0_b32 s84, 0
	s_cselect_b64 s[6:7], -1, 0
	s_or_b64 s[6:7], s[42:43], s[6:7]
	s_xor_b32 s8, s85, 0x78
	s_and_b64 s[6:7], s[6:7], exec
	s_cselect_b32 s9, s85, s8
	s_mov_b64 s[6:7], s[0:1]
	s_and_b32 s87, s9, 7
	s_bfe_u32 s8, s9, 0x40003
	s_lshl_b32 s10, s9, 4
	s_waitcnt vmcnt(22)
	v_cvt_f32_ubyte0_e32 v0, s87
	s_barrier
	v_mbcnt_lo_u32_b32 v1, -1, 0
	v_mbcnt_hi_u32_b32 v1, -1, v1
	s_load_dwordx2 s[6:7], s[6:7], 0x18
	s_and_b32 s10, s10, 0xfffff800
	s_lshl_b32 s11, s8, 7
	v_sub_f32_e32 v32, 0xc0a00000, v0
	s_or_b32 s86, s11, s10
	v_cmp_gt_f32_e32 vcc, s46, v32
	s_and_b64 s[56:57], vcc, exec
	s_cselect_b32 s10, 0xffffffc0, 0
	s_lshl_b32 s30, s87, 9
	s_waitcnt lgkmcnt(0)
	s_add_u32 s6, s6, s30
	s_addc_u32 s7, s7, 0
	s_add_i32 s30, s86, s3
	v_ashrrev_i32_e32 v0, 2, v1
	v_and_or_b32 v1, v1, 15, s30
	v_and_b32_e32 v0, -4, v0
	v_mad_i64_i32 v[2:3], s[56:57], v1, s59, v[84:85]
	s_lshl_b32 s30, s87, 8
	v_lshl_add_u64 v[2:3], v[2:3], 0, s[30:31]
	v_ashrrev_i32_e32 v1, 31, v0
	v_lshl_add_u64 v[34:35], v[0:1], 2, s[6:7]
	v_lshl_add_u64 v[0:1], v[0:1], 1, v[2:3]
	v_cndmask_b32_e32 v33, 0, v118, vcc
	v_add_co_u32_e32 v38, vcc, s60, v0
	v_lshl_add_u64 v[36:37], v[0:1], 0, s[48:49]
	s_nop 0
	v_addc_co_u32_e32 v39, vcc, 0, v1, vcc
	global_load_dwordx4 v[28:31], v[34:35], off
	global_load_dwordx4 v[24:27], v[34:35], off offset:64
	global_load_dwordx4 v[20:23], v[34:35], off offset:128
	global_load_dwordx4 v[16:19], v[34:35], off offset:192
	global_load_dwordx2 v[100:101], v[36:37], off offset:32
	global_load_dwordx2 v[98:99], v[36:37], off offset:64
	global_load_dwordx2 v[96:97], v[36:37], off offset:96
	global_load_dwordx2 v[94:95], v[36:37], off offset:128
	global_load_dwordx4 v[12:15], v[34:35], off offset:256
	global_load_dwordx4 v[8:11], v[34:35], off offset:320
	global_load_dwordx4 v[4:7], v[34:35], off offset:384
	global_load_dwordx4 v[0:3], v[34:35], off offset:448
	global_load_dwordx2 v[102:103], v[38:39], off offset:2048
	global_load_dwordx2 v[92:93], v[36:37], off offset:160
	global_load_dwordx2 v[90:91], v[36:37], off offset:192
	global_load_dwordx2 v[88:89], v[36:37], off offset:224
	v_mbcnt_lo_u32_b32 v34, -1, 0
	v_mbcnt_hi_u32_b32 v34, -1, v34
	s_add_u32 s6, s38, s30
	v_add_u32_e32 v60, s58, v34
	v_lshlrev_b32_e32 v34, 3, v34
	v_and_b32_e32 v34, 56, v34
	s_addc_u32 s7, s39, 0
	v_lshlrev_b32_e32 v86, 1, v34
	v_lshlrev_b32_e32 v34, 3, v34
	v_mov_b32_e32 v35, v87
	v_ashrrev_i32_e32 v108, 3, v60
	v_lshl_add_u64 v[58:59], s[6:7], 0, v[86:87]
	v_lshl_add_u64 v[66:67], s[12:13], 0, v[34:35]
	v_add_u32_e32 v34, s86, v108
	v_mad_i64_i32 v[38:39], s[6:7], v34, s59, v[58:59]
	v_add_u32_e32 v42, s11, v108
	global_load_dwordx4 v[34:37], v[38:39], off
	s_nop 0
	global_load_dwordx4 v[38:41], v[38:39], off offset:128
	v_ashrrev_i32_e32 v43, 31, v42
	v_lshlrev_b64 v[42:43], 9, v[42:43]
	v_lshl_add_u64 v[54:55], v[66:67], 0, v[42:43]
	global_load_dwordx4 v[42:45], v[54:55], off
	global_load_dwordx4 v[46:49], v[54:55], off offset:16
	global_load_dwordx4 v[50:53], v[54:55], off offset:32
	s_nop 0
	global_load_dwordx4 v[54:57], v[54:55], off offset:48
	v_add_u32_e32 v60, 0x200, v60
	v_ashrrev_i32_e32 v109, 3, v60
	v_add_u32_e32 v68, s11, v109
	v_add_u32_e32 v60, s86, v109
	v_ashrrev_i32_e32 v69, 31, v68
	v_mad_i64_i32 v[62:63], s[6:7], v60, s59, v[58:59]
	v_lshlrev_b64 v[68:69], 9, v[68:69]
	global_load_dwordx4 v[58:61], v[62:63], off
	s_nop 0
	global_load_dwordx4 v[62:65], v[62:63], off offset:128
	v_lshl_add_u64 v[78:79], v[66:67], 0, v[68:69]
	global_load_dwordx4 v[66:69], v[78:79], off
	global_load_dwordx4 v[70:73], v[78:79], off offset:16
	global_load_dwordx4 v[74:77], v[78:79], off offset:48
	s_nop 0
	global_load_dwordx4 v[78:81], v[78:79], off offset:32
	v_or_b32_e32 v110, 0x80, v86
	s_add_u32 s6, s34, s30
	s_addc_u32 s7, s35, 0
	v_add_f32_e32 v32, v32, v33
	v_exp_f32_e32 v32, v32
	s_and_b32 s9, s9, 0xffffff80
	s_waitcnt vmcnt(11)
	v_lshlrev_b32_e32 v82, 16, v34
	s_waitcnt vmcnt(10)
	v_lshlrev_b32_e32 v104, 16, v38
	v_and_b32_e32 v105, 0xffff0000, v38
	s_waitcnt vmcnt(9)
	v_mov_b32_e32 v106, v42
	v_mov_b32_e32 v107, v44
	v_mov_b32_e32 v44, v43
	v_and_b32_e32 v83, 0xffff0000, v34
	v_pk_mul_f32 v[42:43], v[44:45], v[104:105]
	v_pk_mul_f32 v[104:105], v[106:107], v[104:105]
	v_pk_fma_f32 v[42:43], v[106:107], v[82:83], v[42:43] neg_lo:[0,0,1] neg_hi:[0,0,1]
	v_pk_fma_f32 v[44:45], v[44:45], v[82:83], v[104:105]
	v_lshlrev_b32_e32 v38, 16, v39
	v_and_b32_e32 v39, 0xffff0000, v39
	s_waitcnt vmcnt(8)
	v_mov_b32_e32 v82, v46
	v_mov_b32_e32 v83, v48
	v_mov_b32_e32 v48, v47
	v_lshlrev_b32_e32 v34, 16, v35
	v_and_b32_e32 v35, 0xffff0000, v35
	v_pk_mul_f32 v[46:47], v[48:49], v[38:39]
	v_pk_mul_f32 v[38:39], v[82:83], v[38:39]
	v_pk_fma_f32 v[46:47], v[82:83], v[34:35], v[46:47] neg_lo:[0,0,1] neg_hi:[0,0,1]
	v_pk_fma_f32 v[38:39], v[48:49], v[34:35], v[38:39]
	v_lshlrev_b32_e32 v48, 16, v40
	v_and_b32_e32 v49, 0xffff0000, v40
	s_waitcnt vmcnt(7)
	v_mov_b32_e32 v82, v50
	v_mov_b32_e32 v83, v52
	v_mov_b32_e32 v52, v51
	v_lshlrev_b32_e32 v34, 16, v36
	v_and_b32_e32 v35, 0xffff0000, v36
	v_pk_mul_f32 v[50:51], v[52:53], v[48:49]
	v_pk_mul_f32 v[48:49], v[82:83], v[48:49]
	v_pk_fma_f32 v[50:51], v[82:83], v[34:35], v[50:51] neg_lo:[0,0,1] neg_hi:[0,0,1]
	v_pk_fma_f32 v[48:49], v[52:53], v[34:35], v[48:49]
	v_lshlrev_b32_e32 v34, 16, v37
	v_and_b32_e32 v35, 0xffff0000, v37
	v_lshlrev_b32_e32 v36, 16, v41
	v_and_b32_e32 v37, 0xffff0000, v41
	s_waitcnt vmcnt(6)
; DI float bflo(unsigned w) { return __uint_as_float(w << 16); }
; DI float bfhi(unsigned w) { return __uint_as_float(w & 0xffff0000u); }
; DI unsigned pack2(float a, float b) { f32x2 v = {a, b}; bf16x2_t r = __builtin_convertvector(v, bf16x2_t); return __builtin_bit_cast(unsigned, r); }
; DI int lane_id() { int l; asm volatile("v_mbcnt_lo_u32_b32 %0, -1, 0\n\tv_mbcnt_hi_u32_b32 %0, -1, %0" : "=v"(l)); return l; }
; template <bool TRIMG>
; DI void stage_rope(const Ctx& c, unsigned dst, int stride, int t0, int col0, int pos0, float scale, float lg, bool kdec) {
;     const u16* proj = (const u16*)(c.ws + WS_PROJ); const f32x2* rope = (const f32x2*)(c.ws + WS_ROPE); const int tid = c.wid * 64 + lane_id();
; #pragma unroll
;     for (int it = 0; it < 2; ++it) { const int item = tid + it * NTHR, j = item >> 3, pc = item & 7, dd = pc * 8;
;         const u16* rp = proj + (size_t)(t0 + j) * INC + col0 + dd;
;         const u32x4 a = *(const u32x4*)rp, b = *(const u32x4*)(rp + 64);
;         const f32x4* cs = (const f32x4*)(rope + (size_t)(pos0 + j) * 64 + dd);
;         const f32x4 c0 = cs[0], c1 = cs[1], c2 = cs[2], c3 = cs[3];
;         const float sc = kdec ? scale * __expf((float)(127 - j) * lg) : scale;
;         float x1[8] = {bflo(a.x), bfhi(a.x), bflo(a.y), bfhi(a.y), bflo(a.z), bfhi(a.z), bflo(a.w), bfhi(a.w)};
;         float x2[8] = {bflo(b.x), bfhi(b.x), bflo(b.y), bfhi(b.y), bflo(b.z), bfhi(b.z), bflo(b.w), bfhi(b.w)};
;         const float cc[8] = {c0[0], c0[2], c1[0], c1[2], c2[0], c2[2], c3[0], c3[2]};
;         const float ss[8] = {c0[1], c0[3], c1[1], c1[3], c2[1], c2[3], c3[1], c3[3]};
;         float o1[8], o2[8];
; #pragma unroll
;         for (int k = 0; k < 8; ++k) { o1[k] = (x1[k] * cc[k] - x2[k] * ss[k]) * sc; o2[k] = (x1[k] * ss[k] + x2[k] * cc[k]) * sc; }
;         const int row = TRIMG ? trrow(j) : j;
;         *LP(u32x4, dst + row * stride + dd * 2) = (u32x4){pack2(o1[0], o1[1]), pack2(o1[2], o1[3]), pack2(o1[4], o1[5]), pack2(o1[6], o1[7])};
;         *LP(u32x4, dst + row * stride + (64 + dd) * 2) = (u32x4){pack2(o2[0], o2[1]), pack2(o2[2], o2[3]), pack2(o2[4], o2[5]), pack2(o2[6], o2[7])}; }
	v_mov_b32_e32 v40, v54
	v_mov_b32_e32 v41, v56
	v_mov_b32_e32 v56, v55
	v_pk_mul_f32 v[52:53], v[56:57], v[36:37]
	v_pk_mul_f32 v[36:37], v[40:41], v[36:37]
	v_pk_fma_f32 v[52:53], v[40:41], v[34:35], v[52:53] neg_lo:[0,0,1] neg_hi:[0,0,1]
	v_pk_fma_f32 v[40:41], v[56:57], v[34:35], v[36:37]
	v_cvt_pk_bf16_f32 v34, v42, v43
	v_mul_lo_u32 v42, v108, s61
	v_add_u32_e32 v42, 0, v42
	v_cvt_pk_bf16_f32 v35, v46, v47
	v_cvt_pk_bf16_f32 v36, v50, v51
	v_cvt_pk_bf16_f32 v37, v52, v53
	v_add_u32_e32 v43, v42, v86
	ds_write_b128 v43, v[34:37]
	v_cvt_pk_bf16_f32 v34, v44, v45
	v_cvt_pk_bf16_f32 v35, v38, v39
	v_cvt_pk_bf16_f32 v36, v48, v49
	v_cvt_pk_bf16_f32 v37, v40, v41
	v_add_u32_e32 v38, v110, v42
	ds_write_b128 v38, v[34:37]
	s_waitcnt vmcnt(4)
	v_lshlrev_b32_e32 v36, 16, v62
	v_and_b32_e32 v37, 0xffff0000, v62
	s_waitcnt vmcnt(3)
	v_mov_b32_e32 v38, v66
	v_mov_b32_e32 v39, v68
	v_mov_b32_e32 v68, v67
	v_lshlrev_b32_e32 v34, 16, v58
	v_and_b32_e32 v35, 0xffff0000, v58
	v_pk_mul_f32 v[40:41], v[68:69], v[36:37]
	v_pk_mul_f32 v[36:37], v[38:39], v[36:37]
	v_pk_fma_f32 v[40:41], v[38:39], v[34:35], v[40:41] neg_lo:[0,0,1] neg_hi:[0,0,1]
	v_pk_fma_f32 v[38:39], v[68:69], v[34:35], v[36:37]
	v_lshlrev_b32_e32 v36, 16, v63
	v_and_b32_e32 v37, 0xffff0000, v63
	s_waitcnt vmcnt(2)
	v_mov_b32_e32 v42, v70
	v_mov_b32_e32 v43, v72
	v_mov_b32_e32 v72, v71
	v_lshlrev_b32_e32 v34, 16, v59
	v_and_b32_e32 v35, 0xffff0000, v59
	v_pk_mul_f32 v[44:45], v[72:73], v[36:37]
	v_pk_mul_f32 v[36:37], v[42:43], v[36:37]
	v_pk_fma_f32 v[44:45], v[42:43], v[34:35], v[44:45] neg_lo:[0,0,1] neg_hi:[0,0,1]
	v_pk_fma_f32 v[42:43], v[72:73], v[34:35], v[36:37]
	v_lshlrev_b32_e32 v36, 16, v64
	v_and_b32_e32 v37, 0xffff0000, v64
	s_waitcnt vmcnt(0)
	v_mov_b32_e32 v46, v78
	v_mov_b32_e32 v47, v80
	v_mov_b32_e32 v80, v79
	v_lshlrev_b32_e32 v34, 16, v60
	v_and_b32_e32 v35, 0xffff0000, v60
	v_pk_mul_f32 v[48:49], v[80:81], v[36:37]
	v_pk_mul_f32 v[36:37], v[46:47], v[36:37]
	v_pk_fma_f32 v[48:49], v[46:47], v[34:35], v[48:49] neg_lo:[0,0,1] neg_hi:[0,0,1]
	v_pk_fma_f32 v[46:47], v[80:81], v[34:35], v[36:37]
	v_lshlrev_b32_e32 v36, 16, v65
	v_and_b32_e32 v37, 0xffff0000, v65
	v_mov_b32_e32 v50, v74
	v_mov_b32_e32 v51, v76
	v_mov_b32_e32 v76, v75
	v_lshlrev_b32_e32 v34, 16, v61
	v_and_b32_e32 v35, 0xffff0000, v61
	v_pk_mul_f32 v[52:53], v[76:77], v[36:37]
	v_pk_mul_f32 v[36:37], v[50:51], v[36:37]
	v_pk_fma_f32 v[52:53], v[50:51], v[34:35], v[52:53] neg_lo:[0,0,1] neg_hi:[0,0,1]
	v_pk_fma_f32 v[50:51], v[76:77], v[34:35], v[36:37]
	v_cvt_pk_bf16_f32 v34, v40, v41
	v_mul_lo_u32 v40, v109, s61
	v_add_u32_e32 v40, 0, v40
	v_cvt_pk_bf16_f32 v35, v44, v45
	v_cvt_pk_bf16_f32 v36, v48, v49
	v_cvt_pk_bf16_f32 v37, v52, v53
	v_add_u32_e32 v41, v40, v86
	ds_write_b128 v41, v[34:37]
	v_cvt_pk_bf16_f32 v34, v38, v39
	v_cvt_pk_bf16_f32 v35, v42, v43
	v_cvt_pk_bf16_f32 v36, v46, v47
	v_cvt_pk_bf16_f32 v37, v50, v51
	v_add_u32_e32 v38, v40, v110
	ds_write_b128 v38, v[34:37]
	v_mbcnt_lo_u32_b32 v34, -1, 0
	v_mbcnt_hi_u32_b32 v34, -1, v34
	s_nop 0
	v_add_u32_e32 v60, s58, v34
	v_lshlrev_b32_e32 v34, 3, v34
	v_and_b32_e32 v36, 56, v34
	v_lshlrev_b32_e32 v86, 1, v36
	v_lshl_add_u64 v[34:35], s[6:7], 0, v[86:87]
	v_lshl_add_u64 v[58:59], v[34:35], 0, s[50:51]
	v_lshlrev_b32_e32 v34, 3, v36
	v_mov_b32_e32 v35, v87
	v_ashrrev_i32_e32 v104, 3, v60
	v_lshl_add_u64 v[66:67], s[12:13], 0, v[34:35]
	v_add_u32_e32 v34, s86, v104
	v_mad_i64_i32 v[38:39], s[56:57], v34, s59, v[58:59]
	v_add_u32_e32 v42, s11, v104
	global_load_dwordx4 v[34:37], v[38:39], off
	s_nop 0
	global_load_dwordx4 v[38:41], v[38:39], off offset:128
	v_ashrrev_i32_e32 v43, 31, v42
	v_lshlrev_b64 v[42:43], 9, v[42:43]
	v_lshl_add_u64 v[54:55], v[66:67], 0, v[42:43]
	global_load_dwordx4 v[42:45], v[54:55], off
	global_load_dwordx4 v[46:49], v[54:55], off offset:16
	global_load_dwordx4 v[50:53], v[54:55], off offset:32
	s_nop 0
	global_load_dwordx4 v[54:57], v[54:55], off offset:48
	v_add_u32_e32 v60, 0x200, v60
	v_ashrrev_i32_e32 v105, 3, v60
	v_add_u32_e32 v68, s11, v105
	v_add_u32_e32 v60, s86, v105
	v_ashrrev_i32_e32 v69, 31, v68
	v_mad_i64_i32 v[62:63], s[56:57], v60, s59, v[58:59]
	v_lshlrev_b64 v[68:69], 9, v[68:69]
	global_load_dwordx4 v[58:61], v[62:63], off
	s_nop 0
	global_load_dwordx4 v[62:65], v[62:63], off offset:128
	v_lshl_add_u64 v[74:75], v[66:67], 0, v[68:69]
	global_load_dwordx4 v[66:69], v[74:75], off
	global_load_dwordx4 v[70:73], v[74:75], off offset:16
	v_or_b32_e32 v106, 0x80, v86
	s_waitcnt vmcnt(9)
	v_lshlrev_b32_e32 v76, 16, v34
	s_waitcnt vmcnt(8)
	v_lshlrev_b32_e32 v78, 16, v38
	v_and_b32_e32 v79, 0xffff0000, v38
	s_waitcnt vmcnt(7)
	v_mov_b32_e32 v81, v44
	v_mov_b32_e32 v44, v43
	v_and_b32_e32 v77, 0xffff0000, v34
	v_mov_b32_e32 v80, v42
	v_pk_mul_f32 v[42:43], v[44:45], v[78:79]
	v_lshlrev_b32_e32 v38, 16, v39
	v_pk_fma_f32 v[42:43], v[80:81], v[76:77], v[42:43] neg_lo:[0,0,1] neg_hi:[0,0,1]
	v_and_b32_e32 v39, 0xffff0000, v39
	v_pk_mul_f32 v[82:83], v[42:43], s[52:53] op_sel_hi:[1,0]
	v_pk_mul_f32 v[42:43], v[80:81], v[78:79]
	s_waitcnt vmcnt(6)
	v_mov_b32_e32 v80, v46
	v_pk_fma_f32 v[42:43], v[44:45], v[76:77], v[42:43]
	v_mov_b32_e32 v81, v48
	v_pk_mul_f32 v[78:79], v[42:43], s[52:53] op_sel_hi:[1,0]
	global_load_dwordx4 v[42:45], v[74:75], off offset:48
	s_nop 0
	global_load_dwordx4 v[74:77], v[74:75], off offset:32
	v_mov_b32_e32 v48, v47
	v_lshlrev_b32_e32 v34, 16, v35
	v_and_b32_e32 v35, 0xffff0000, v35
	v_pk_mul_f32 v[46:47], v[48:49], v[38:39]
	v_pk_mul_f32 v[38:39], v[80:81], v[38:39]
	v_pk_fma_f32 v[46:47], v[80:81], v[34:35], v[46:47] neg_lo:[0,0,1] neg_hi:[0,0,1]
	v_pk_fma_f32 v[34:35], v[48:49], v[34:35], v[38:39]
	v_lshlrev_b32_e32 v48, 16, v40
	v_and_b32_e32 v49, 0xffff0000, v40
	s_waitcnt vmcnt(7)
; DI float bflo(unsigned w) { return __uint_as_float(w << 16); }
; template <bool TRIMG>
; DI void stage_rope(const Ctx& c, unsigned dst, int stride, int t0, int col0, int pos0, float scale, float lg, bool kdec) {
;     const u16* proj = (const u16*)(c.ws + WS_PROJ); const f32x2* rope = (const f32x2*)(c.ws + WS_ROPE); const int tid = c.wid * 64 + lane_id();
; #pragma unroll
;     for (int it = 0; it < 2; ++it) { const int item = tid + it * NTHR, j = item >> 3, pc = item & 7, dd = pc * 8;
;         const u16* rp = proj + (size_t)(t0 + j) * INC + col0 + dd;
;         const u32x4 a = *(const u32x4*)rp, b = *(const u32x4*)(rp + 64);
;         const f32x4* cs = (const f32x4*)(rope + (size_t)(pos0 + j) * 64 + dd);
;         const f32x4 c0 = cs[0], c1 = cs[1], c2 = cs[2], c3 = cs[3];
;         const float sc = kdec ? scale * __expf((float)(127 - j) * lg) : scale;
;         float x1[8] = {bflo(a.x), bfhi(a.x), bflo(a.y), bfhi(a.y), bflo(a.z), bfhi(a.z), bflo(a.w), bfhi(a.w)};
;         float x2[8] = {bflo(b.x), bfhi(b.x), bflo(b.y), bfhi(b.y), bflo(b.z), bfhi(b.z), bflo(b.w), bfhi(b.w)};
;         const float cc[8] = {c0[0], c0[2], c1[0], c1[2], c2[0], c2[2], c3[0], c3[2]};
;         const float ss[8] = {c0[1], c0[3], c1[1], c1[3], c2[1], c2[3], c3[1], c3[3]};
;         float o1[8], o2[8];
; #pragma unroll
;         for (int k = 0; k < 8; ++k) { o1[k] = (x1[k] * cc[k] - x2[k] * ss[k]) * sc; o2[k] = (x1[k] * ss[k] + x2[k] * cc[k]) * sc; }
;         const int row = TRIMG ? trrow(j) : j;
;         *LP(u32x4, dst + row * stride + dd * 2) = (u32x4){pack2(o1[0], o1[1]), pack2(o1[2], o1[3]), pack2(o1[4], o1[5]), pack2(o1[6], o1[7])};
;         *LP(u32x4, dst + row * stride + (64 + dd) * 2) = (u32x4){pack2(o2[0], o2[1]), pack2(o2[2], o2[3]), pack2(o2[4], o2[5]), pack2(o2[6], o2[7])}; }
; }
; template <bool TRIMG>
; DI void stage_plain(const Ctx& c, unsigned dst, int stride, int t0, int col0) {
;     const u16* proj = (const u16*)(c.ws + WS_PROJ); const int tid = c.wid * 64 + lane_id();
; #pragma unroll
;     for (int it = 0; it < 4; ++it) { const int item = tid + it * NTHR, j = item >> 4, ch = item & 15;
;         const u32x4 a = *(const u32x4*)(proj + (size_t)(t0 + j) * INC + col0 + ch * 8);
;         const int row = TRIMG ? trrow(j) : j;
;         *LP(u32x4, dst + row * stride + ch * 16) = a; }
; }
; DI void ret_out_unit(const Ctx& c, int u) {
;     ...
;     {
	v_mov_b32_e32 v80, v50
	v_mov_b32_e32 v81, v52
	v_mov_b32_e32 v52, v51
	v_pk_mul_f32 v[38:39], v[34:35], s[52:53] op_sel_hi:[1,0]
	v_lshlrev_b32_e32 v34, 16, v36
	v_and_b32_e32 v35, 0xffff0000, v36
	v_pk_mul_f32 v[50:51], v[52:53], v[48:49]
	v_pk_mul_f32 v[48:49], v[80:81], v[48:49]
	v_pk_fma_f32 v[50:51], v[80:81], v[34:35], v[50:51] neg_lo:[0,0,1] neg_hi:[0,0,1]
	v_pk_fma_f32 v[34:35], v[52:53], v[34:35], v[48:49]
	v_lshlrev_b32_e32 v36, 16, v41
	v_pk_mul_f32 v[48:49], v[34:35], s[52:53] op_sel_hi:[1,0]
	v_lshlrev_b32_e32 v34, 16, v37
	v_and_b32_e32 v35, 0xffff0000, v37
	v_and_b32_e32 v37, 0xffff0000, v41
	s_waitcnt vmcnt(6)
	v_mov_b32_e32 v40, v54
	v_mov_b32_e32 v41, v56
	v_mov_b32_e32 v56, v55
	v_pk_mul_f32 v[52:53], v[56:57], v[36:37]
	v_pk_mul_f32 v[36:37], v[40:41], v[36:37]
	v_pk_mul_f32 v[46:47], v[46:47], s[52:53] op_sel_hi:[1,0]
	v_pk_fma_f32 v[52:53], v[40:41], v[34:35], v[52:53] neg_lo:[0,0,1] neg_hi:[0,0,1]
	v_pk_fma_f32 v[34:35], v[56:57], v[34:35], v[36:37]
	v_pk_mul_f32 v[50:51], v[50:51], s[52:53] op_sel_hi:[1,0]
	v_pk_mul_f32 v[40:41], v[34:35], s[52:53] op_sel_hi:[1,0]
	v_cvt_pk_bf16_f32 v35, v46, v47
	v_mul_lo_u32 v46, v104, s61
	v_pk_mul_f32 v[52:53], v[52:53], s[52:53] op_sel_hi:[1,0]
	v_add_u32_e32 v46, s62, v46
	v_cvt_pk_bf16_f32 v34, v82, v83
	v_cvt_pk_bf16_f32 v36, v50, v51
	v_cvt_pk_bf16_f32 v37, v52, v53
	v_add_u32_e32 v47, v46, v86
	ds_write_b128 v47, v[34:37]
	v_cvt_pk_bf16_f32 v34, v78, v79
	v_cvt_pk_bf16_f32 v35, v38, v39
	v_cvt_pk_bf16_f32 v36, v48, v49
	v_cvt_pk_bf16_f32 v37, v40, v41
	v_add_u32_e32 v38, v106, v46
	ds_write_b128 v38, v[34:37]
	s_waitcnt vmcnt(4)
	v_lshlrev_b32_e32 v36, 16, v62
	v_and_b32_e32 v37, 0xffff0000, v62
	s_waitcnt vmcnt(3)
	v_mov_b32_e32 v38, v66
	v_mov_b32_e32 v39, v68
	v_mov_b32_e32 v68, v67
	v_lshlrev_b32_e32 v34, 16, v58
	v_and_b32_e32 v35, 0xffff0000, v58
	v_pk_mul_f32 v[40:41], v[68:69], v[36:37]
	v_pk_mul_f32 v[36:37], v[38:39], v[36:37]
	v_pk_fma_f32 v[40:41], v[38:39], v[34:35], v[40:41] neg_lo:[0,0,1] neg_hi:[0,0,1]
	v_pk_fma_f32 v[34:35], v[68:69], v[34:35], v[36:37]
	v_lshlrev_b32_e32 v36, 16, v63
	v_and_b32_e32 v37, 0xffff0000, v63
	s_waitcnt vmcnt(2)
	v_mov_b32_e32 v46, v70
	v_mov_b32_e32 v47, v72
	v_mov_b32_e32 v72, v71
	v_pk_mul_f32 v[38:39], v[34:35], s[52:53] op_sel_hi:[1,0]
	v_lshlrev_b32_e32 v34, 16, v59
	v_and_b32_e32 v35, 0xffff0000, v59
	v_pk_mul_f32 v[48:49], v[72:73], v[36:37]
	v_pk_mul_f32 v[36:37], v[46:47], v[36:37]
	v_pk_fma_f32 v[48:49], v[46:47], v[34:35], v[48:49] neg_lo:[0,0,1] neg_hi:[0,0,1]
	v_pk_fma_f32 v[34:35], v[72:73], v[34:35], v[36:37]
	v_lshlrev_b32_e32 v36, 16, v64
	v_and_b32_e32 v37, 0xffff0000, v64
	v_pk_mul_f32 v[46:47], v[34:35], s[52:53] op_sel_hi:[1,0]
	v_lshlrev_b32_e32 v34, 16, v60
	v_and_b32_e32 v35, 0xffff0000, v60
	v_pk_mul_f32 v[40:41], v[40:41], s[52:53] op_sel_hi:[1,0]
	s_waitcnt vmcnt(1)
	v_mov_b32_e32 v54, v42
	s_waitcnt vmcnt(0)
	v_mov_b32_e32 v50, v74
	v_mov_b32_e32 v51, v76
	v_mov_b32_e32 v76, v75
	v_pk_mul_f32 v[52:53], v[76:77], v[36:37]
	v_pk_mul_f32 v[36:37], v[50:51], v[36:37]
	v_pk_fma_f32 v[52:53], v[50:51], v[34:35], v[52:53] neg_lo:[0,0,1] neg_hi:[0,0,1]
	v_pk_fma_f32 v[34:35], v[76:77], v[34:35], v[36:37]
	v_lshlrev_b32_e32 v36, 16, v65
	v_and_b32_e32 v37, 0xffff0000, v65
	v_mov_b32_e32 v55, v44
	v_mov_b32_e32 v44, v43
	v_pk_mul_f32 v[50:51], v[34:35], s[52:53] op_sel_hi:[1,0]
	v_lshlrev_b32_e32 v34, 16, v61
	v_and_b32_e32 v35, 0xffff0000, v61
	v_pk_mul_f32 v[42:43], v[44:45], v[36:37]
	v_pk_mul_f32 v[36:37], v[54:55], v[36:37]
	v_pk_fma_f32 v[42:43], v[54:55], v[34:35], v[42:43] neg_lo:[0,0,1] neg_hi:[0,0,1]
	v_pk_fma_f32 v[34:35], v[44:45], v[34:35], v[36:37]
	v_pk_mul_f32 v[48:49], v[48:49], s[52:53] op_sel_hi:[1,0]
	v_pk_mul_f32 v[44:45], v[34:35], s[52:53] op_sel_hi:[1,0]
	v_cvt_pk_bf16_f32 v34, v40, v41
	v_mul_lo_u32 v40, v105, s61
	v_pk_mul_f32 v[52:53], v[52:53], s[52:53] op_sel_hi:[1,0]
	v_pk_mul_f32 v[42:43], v[42:43], s[52:53] op_sel_hi:[1,0]
	v_add_u32_e32 v40, s62, v40
	v_cvt_pk_bf16_f32 v35, v48, v49
	v_cvt_pk_bf16_f32 v36, v52, v53
	v_cvt_pk_bf16_f32 v37, v42, v43
	v_add_u32_e32 v41, v40, v86
	ds_write_b128 v41, v[34:37]
	v_cvt_pk_bf16_f32 v34, v38, v39
	v_cvt_pk_bf16_f32 v35, v46, v47
	v_cvt_pk_bf16_f32 v36, v50, v51
	v_cvt_pk_bf16_f32 v37, v44, v45
	v_add_u32_e32 v38, v40, v106
	ds_write_b128 v38, v[34:37]
	v_mbcnt_lo_u32_b32 v34, -1, 0
	v_mbcnt_hi_u32_b32 v34, -1, v34
	v_ldexp_f32 v80, v32, s10
	v_add_u32_e32 v48, s58, v34
	v_lshlrev_b32_e32 v34, 4, v34
	v_and_b32_e32 v86, 0xf0, v34
	v_lshl_add_u64 v[34:35], s[6:7], 0, v[86:87]
	v_ashrrev_i32_e32 v50, 4, v48
	v_lshl_add_u64 v[46:47], v[34:35], 0, s[54:55]
	v_add_u32_e32 v34, s86, v50
	v_mad_i64_i32 v[34:35], s[6:7], v34, s59, v[46:47]
	v_add_u32_e32 v38, 0x200, v48
	global_load_dwordx4 v[34:37], v[34:35], off
	v_ashrrev_i32_e32 v52, 4, v38
	v_add_u32_e32 v38, s86, v52
	v_mad_i64_i32 v[38:39], s[6:7], v38, s59, v[46:47]
	v_add_u32_e32 v42, 0x400, v48
	global_load_dwordx4 v[38:41], v[38:39], off
	v_ashrrev_i32_e32 v53, 4, v42
	v_add_u32_e32 v42, s86, v53
	v_mad_i64_i32 v[42:43], s[6:7], v42, s59, v[46:47]
	global_load_dwordx4 v[42:45], v[42:43], off
	v_add_u32_e32 v48, 0x600, v48
	v_ashrrev_i32_e32 v54, 4, v48
	v_add_u32_e32 v48, s86, v54
	v_mad_i64_i32 v[46:47], s[6:7], v48, s59, v[46:47]
	global_load_dwordx4 v[46:49], v[46:47], off
	v_sub_f32_e32 v33, 1.0, v80
	v_frexp_mant_f32_e32 v32, v33
	v_lshrrev_b32_e32 v51, 1, v50
	v_cmp_gt_f32_e64 s[6:7], s47, v32
	v_add_u32_e32 v32, s63, v86
	v_bitop3_b32 v50, v51, v50, 4 bitop3:0x6c
	v_mad_u64_u32 v[50:51], s[10:11], v50, s64, v[32:33]
	s_waitcnt vmcnt(3)
	ds_write_b128 v50, v[34:37]
	v_lshrrev_b32_e32 v34, 1, v52
	v_bitop3_b32 v34, v34, v52, 4 bitop3:0x6c
	v_mad_u64_u32 v[34:35], s[10:11], v34, s64, v[32:33]
	s_waitcnt vmcnt(2)
	ds_write_b128 v34, v[38:41]
	v_lshrrev_b32_e32 v34, 1, v53
	v_bitop3_b32 v34, v34, v53, 4 bitop3:0x6c
	v_mad_u64_u32 v[34:35], s[10:11], v34, s64, v[32:33]
	s_waitcnt vmcnt(1)
	ds_write_b128 v34, v[42:45]
	v_lshrrev_b32_e32 v34, 1, v54
	v_bitop3_b32 v34, v34, v54, 4 bitop3:0x6c
	v_mad_u64_u32 v[34:35], s[10:11], v34, s64, v[32:33]
	s_lshl_b32 s10, s87, 4
	s_or_b32 s9, s10, s9
	s_or_b32 s10, s9, s8
	s_ashr_i32 s11, s10, 31
	s_lshl_b64 s[10:11], s[10:11], 15
	s_add_u32 s10, s4, s10
	s_addc_u32 s11, s5, s11
	s_cmp_lg_u32 s8, 0
	s_waitcnt vmcnt(0)
	ds_write_b128 v34, v[46:49]
	v_mbcnt_lo_u32_b32 v32, -1, 0
	v_mbcnt_hi_u32_b32 v32, -1, v32
	s_cselect_b64 s[56:57], -1, 0
	s_cmp_eq_u32 s8, 0
	v_add_u32_e32 v34, s58, v32
	s_cbranch_scc1 .Lstate_nopre
; DI int lane_id() { int l; asm volatile("v_mbcnt_lo_u32_b32 %0, -1, 0\n\tv_mbcnt_hi_u32_b32 %0, -1, %0" : "=v"(l)); return l; }
; DI void ret_out_unit(const Ctx& c, int u) {
;     ...
;     {
;         const u32x2* sc = (const u32x2*)((const u16*)(c.ws + WS_KV) + (size_t)512 * 16384 + (size_t)((b * NHEAD + h) * NCH + n) * 16384); const int tid = c.wid * 64 + lane_id();
; #pragma unroll
;         for (int i = 0; i < 8; ++i) { const int idx = tid + i * NTHR, dd = idx >> 5, e4 = (idx & 31) * 4;
;             const u32x2 sv = (n > 0) ? sc[idx] : (u32x2){0u, 0u};
;             *LP(u32x2, Simg + trrow(dd) * TS + e4 * 2) = sv; }
	v_mov_b32_e32 v64, v34
	v_ashrrev_i32_e32 v65, 31, v64
	v_lshl_add_u64 v[64:65], v[64:65], 3, s[10:11]
	global_load_dwordx2 v[44:45], v[64:65], off
	v_add_u32_e32 v66, 0x200, v34
	v_ashrrev_i32_e32 v67, 31, v66
	v_lshl_add_u64 v[66:67], v[66:67], 3, s[10:11]
	global_load_dwordx2 v[46:47], v[66:67], off
	v_add_u32_e32 v68, 0x400, v34
	v_ashrrev_i32_e32 v69, 31, v68
	v_lshl_add_u64 v[68:69], v[68:69], 3, s[10:11]
	global_load_dwordx2 v[48:49], v[68:69], off
	v_add_u32_e32 v70, 0x600, v34
	v_ashrrev_i32_e32 v71, 31, v70
	v_lshl_add_u64 v[70:71], v[70:71], 3, s[10:11]
	global_load_dwordx2 v[52:53], v[70:71], off
	v_add_u32_e32 v72, 0x800, v34
	v_ashrrev_i32_e32 v73, 31, v72
	v_lshl_add_u64 v[72:73], v[72:73], 3, s[10:11]
	global_load_dwordx2 v[54:55], v[72:73], off
	v_add_u32_e32 v74, 0xa00, v34
	v_ashrrev_i32_e32 v75, 31, v74
	v_lshl_add_u64 v[74:75], v[74:75], 3, s[10:11]
	global_load_dwordx2 v[56:57], v[74:75], off
	v_add_u32_e32 v76, 0xc00, v34
	v_ashrrev_i32_e32 v77, 31, v76
	v_lshl_add_u64 v[76:77], v[76:77], 3, s[10:11]
	global_load_dwordx2 v[58:59], v[76:77], off
	v_add_u32_e32 v82, 0xe00, v34
	v_ashrrev_i32_e32 v83, 31, v82
	v_lshl_add_u64 v[82:83], v[82:83], 3, s[10:11]
	global_load_dwordx2 v[60:61], v[82:83], off
.Lstate_nopre:
	s_cbranch_scc1 .LBB0_275
	v_ashrrev_i32_e32 v35, 31, v34
	v_lshl_add_u64 v[36:37], v[34:35], 3, s[10:11]
	s_waitcnt vmcnt(0)
	v_mov_b32_e32 v36, v44
	v_mov_b32_e32 v37, v45
	s_branch .LBB0_276

; DI int lane_id() { int l; asm volatile("v_mbcnt_lo_u32_b32 %0, -1, 0\n\tv_mbcnt_hi_u32_b32 %0, -1, %0" : "=v"(l)); return l; }
; DI void ret_out_unit(const Ctx& c, int u) {
;     ...
;     {
;         const u32x2* sc = (const u32x2*)((const u16*)(c.ws + WS_KV) + (size_t)512 * 16384 + (size_t)((b * NHEAD + h) * NCH + n) * 16384); const int tid = c.wid * 64 + lane_id();
; #pragma unroll
;         for (int i = 0; i < 8; ++i) { const int idx = tid + i * NTHR, dd = idx >> 5, e4 = (idx & 31) * 4;
;             const u32x2 sv = (n > 0) ? sc[idx] : (u32x2){0u, 0u};
;             *LP(u32x2, Simg + trrow(dd) * TS + e4 * 2) = sv; }
.LBB0_276:
	v_lshlrev_b32_e32 v32, 3, v32
	v_ashrrev_i32_e32 v35, 5, v34
	v_and_b32_e32 v32, 0xf8, v32
	v_lshrrev_b32_e32 v38, 1, v35
	v_add_u32_e32 v32, s65, v32
	v_bitop3_b32 v35, v38, v35, 4 bitop3:0x6c
	v_mad_u64_u32 v[38:39], s[8:9], v35, s64, v[32:33]
	v_cndmask_b32_e64 v35, 0, 1, s[56:57]
	s_waitcnt vmcnt(0)
	ds_write_b64 v38, v[36:37]
	v_add_u32_e32 v38, 0x200, v34
	v_mov_b32_e32 v36, 0
	v_cmp_ne_u32_e64 s[8:9], 1, v35
	s_andn2_b64 vcc, exec, s[56:57]
	v_mov_b32_e32 v40, 0
	v_mov_b32_e32 v41, 0
	s_cbranch_vccnz .LBB0_278
	v_ashrrev_i32_e32 v39, 31, v38
	v_lshl_add_u64 v[40:41], v[38:39], 3, s[10:11]
	v_mov_b32_e32 v40, v46
	v_mov_b32_e32 v41, v47
.LBB0_278:
	v_ashrrev_i32_e32 v35, 5, v38
	v_lshrrev_b32_e32 v37, 1, v35
	v_bitop3_b32 v35, v37, v35, 4 bitop3:0x6c
	v_mad_u64_u32 v[38:39], s[56:57], v35, s64, v[32:33]
	s_waitcnt vmcnt(0)
	ds_write_b64 v38, v[40:41]
	v_add_u32_e32 v38, 0x400, v34
	s_and_b64 vcc, exec, s[8:9]
	v_mov_b32_e32 v37, 0
	s_cbranch_vccnz .LBB0_280
	v_ashrrev_i32_e32 v39, 31, v38
	v_lshl_add_u64 v[36:37], v[38:39], 3, s[10:11]
	v_mov_b32_e32 v36, v48
	v_mov_b32_e32 v37, v49
.LBB0_280:
	v_ashrrev_i32_e32 v35, 5, v38
	v_lshrrev_b32_e32 v38, 1, v35
	v_bitop3_b32 v35, v38, v35, 4 bitop3:0x6c
	v_mad_u64_u32 v[38:39], s[56:57], v35, s64, v[32:33]
	s_waitcnt vmcnt(0)
	ds_write_b64 v38, v[36:37]
	v_add_u32_e32 v38, 0x600, v34
	v_mov_b32_e32 v36, 0
	s_and_b64 vcc, exec, s[8:9]
	v_mov_b32_e32 v40, 0
	v_mov_b32_e32 v41, 0
	s_cbranch_vccnz .LBB0_282
	v_ashrrev_i32_e32 v39, 31, v38
	v_lshl_add_u64 v[40:41], v[38:39], 3, s[10:11]
	v_mov_b32_e32 v40, v52
	v_mov_b32_e32 v41, v53
.LBB0_282:
	v_ashrrev_i32_e32 v35, 5, v38
	v_lshrrev_b32_e32 v37, 1, v35
	v_bitop3_b32 v35, v37, v35, 4 bitop3:0x6c
	v_mad_u64_u32 v[38:39], s[56:57], v35, s64, v[32:33]
	s_waitcnt vmcnt(0)
	ds_write_b64 v38, v[40:41]
	v_add_u32_e32 v38, 0x800, v34
	s_and_b64 vcc, exec, s[8:9]
	v_mov_b32_e32 v37, 0
	s_cbranch_vccnz .LBB0_284
	v_ashrrev_i32_e32 v39, 31, v38
	v_lshl_add_u64 v[36:37], v[38:39], 3, s[10:11]
	v_mov_b32_e32 v36, v54
	v_mov_b32_e32 v37, v55
.LBB0_284:
	v_ashrrev_i32_e32 v35, 5, v38
	v_lshrrev_b32_e32 v38, 1, v35
	v_bitop3_b32 v35, v38, v35, 4 bitop3:0x6c
	v_mad_u64_u32 v[38:39], s[56:57], v35, s64, v[32:33]
	s_waitcnt vmcnt(0)
	ds_write_b64 v38, v[36:37]
	v_add_u32_e32 v38, 0xa00, v34
	v_mov_b32_e32 v36, 0
	s_and_b64 vcc, exec, s[8:9]
	v_mov_b32_e32 v40, 0
	v_mov_b32_e32 v41, 0
	s_cbranch_vccnz .LBB0_286
	v_ashrrev_i32_e32 v39, 31, v38
	v_lshl_add_u64 v[40:41], v[38:39], 3, s[10:11]
	v_mov_b32_e32 v40, v56
	v_mov_b32_e32 v41, v57
.LBB0_286:
	v_ashrrev_i32_e32 v35, 5, v38
	v_lshrrev_b32_e32 v37, 1, v35
	v_bitop3_b32 v35, v37, v35, 4 bitop3:0x6c
	v_mad_u64_u32 v[38:39], s[56:57], v35, s64, v[32:33]
	s_waitcnt vmcnt(0)
	ds_write_b64 v38, v[40:41]
	v_add_u32_e32 v38, 0xc00, v34
	s_and_b64 vcc, exec, s[8:9]
	v_mov_b32_e32 v37, 0
	s_cbranch_vccnz .LBB0_288
	v_ashrrev_i32_e32 v39, 31, v38
	v_lshl_add_u64 v[36:37], v[38:39], 3, s[10:11]
	v_mov_b32_e32 v36, v58
	v_mov_b32_e32 v37, v59
.LBB0_288:
	v_cvt_f64_f32_e32 v[40:41], v33
	v_frexp_exp_i32_f64_e32 v35, v[40:41]
	v_subbrev_co_u32_e64 v40, vcc, 0, v35, s[6:7]
	v_ashrrev_i32_e32 v35, 5, v38
	v_lshrrev_b32_e32 v38, 1, v35
	v_bitop3_b32 v35, v38, v35, 4 bitop3:0x6c
	v_mad_u64_u32 v[38:39], s[6:7], v35, s64, v[32:33]
	s_waitcnt vmcnt(0)
	ds_write_b64 v38, v[36:37]
	s_and_b64 vcc, exec, s[8:9]
	v_add_u32_e32 v36, 0xe00, v34
	s_cbranch_vccnz .LBB0_290
	v_ashrrev_i32_e32 v37, 31, v36
	v_lshl_add_u64 v[34:35], v[36:37], 3, s[10:11]
	v_mov_b32_e32 v34, v60
	v_mov_b32_e32 v35, v61
	s_branch .LBB0_291

; #define LAS __attribute__((address_space(3)))
; DI int lane_id() { int l; asm volatile("v_mbcnt_lo_u32_b32 %0, -1, 0\n\tv_mbcnt_hi_u32_b32 %0, -1, %0" : "=v"(l)); return l; }
; DI KPtr kargs() { KPtr p = (KPtr)__builtin_amdgcn_kernarg_segment_ptr(); asm volatile("" : "+s"(p)); return p; }
; DI void p4_ln_router(const Ctx& c) {
;     const KPtr kp = kargs();
;     const int lane = lane_id(), w = c.wid, fq = lane >> 4, fr = lane & 15, tid = c.wid * 64 + lane;
;     const unsigned base = (unsigned)(size_t)c.lds, Xhi = base, Xlo = base + 16 * XSTR;
;     LAS float* red = (LAS float*)c.lds;
;     LAS float* logit = (LAS float*)(c.lds + 135168);
;     LAS int* sel_e = (LAS int*)(c.lds + 135168 + 4096);
;     LAS float* sel_g = (LAS float*)(c.lds + 135168 + 4096 + 512);
;     LAS int* sel_p = (LAS int*)(c.lds + 135168 + 4096 + 1024);
;     LAS unsigned* lcnt = (LAS unsigned*)(c.lds + 135168 + 4096 + 1536);
;     LAS unsigned* gbase = lcnt + 32;
;     const u16* y1 = (const u16*)(c.ws + WS_Y1); const float* lw = kp->in[12]; const float* lb = kp->in[13];
;     const float* wr_ = kp->in[14]; const float* br_ = kp->in[15];
;     u16* x1b = (u16*)(c.ws + WS_X1B); float* st1 = (float*)(c.ws + WS_ST1);
;     for (int tb = c.bid; tb < T / 32; tb += c.G) {
;     ...
;             for (int i = 0; i < 8; ++i) { const int d = (i * 64 + lane) * 4; const f32x4 g = *(const f32x4*)(lw + d), bb = *(const f32x4*)(lb + d);
.LBB0_435:
	s_or_b64 exec, exec, s[6:7]
	s_add_u32 s20, s34, 0x16690000
	s_addc_u32 s21, s35, 0
	s_waitcnt lgkmcnt(0)
	v_cndmask_b32_e64 v0, 0, 1, s[40:41]
	s_add_u32 s3, s34, 0x18690000
	v_cmp_ne_u32_e64 s[4:5], 1, v0
	s_mov_b64 s[8:9], s[0:1]
	s_addc_u32 s71, s35, 0
	v_writelane_b32 v242, s4, 4
	s_andn2_b64 vcc, exec, s[40:41]
	s_barrier
	v_writelane_b32 v242, s5, 5
	v_mbcnt_lo_u32_b32 v0, -1, 0
	v_mbcnt_hi_u32_b32 v0, -1, v0
	s_cbranch_vccnz .LBB0_456
	s_waitcnt vmcnt(18)
	v_mbcnt_hi_u32_b32 v6, -1, v196
	v_and_b32_e32 v1, 64, v6
	v_add_u32_e32 v7, 64, v1
	v_xor_b32_e32 v14, 32, v6
	v_cmp_lt_i32_e32 vcc, v14, v7
	s_load_dwordx8 s[12:19], s[8:9], 0x60
	v_lshlrev_b32_e32 v2, 2, v0
	v_cndmask_b32_e32 v14, v6, v14, vcc
	v_lshlrev_b32_e32 v83, 2, v14
	v_xor_b32_e32 v14, 16, v6
	v_cmp_lt_i32_e32 vcc, v14, v7
	v_ashrrev_i32_e32 v3, 31, v2
	v_lshlrev_b64 v[4:5], 2, v[2:3]
	v_cndmask_b32_e32 v14, v6, v14, vcc
	v_lshlrev_b32_e32 v84, 2, v14
	v_xor_b32_e32 v14, 8, v6
	v_cmp_lt_i32_e32 vcc, v14, v7
	s_waitcnt lgkmcnt(0)
	v_lshl_add_u64 v[28:29], s[12:13], 0, v[4:5]
	v_lshl_add_u64 v[30:31], s[14:15], 0, v[4:5]
	v_cndmask_b32_e32 v14, v6, v14, vcc
	v_lshlrev_b32_e32 v85, 2, v14
	v_xor_b32_e32 v14, 4, v6
	v_cmp_lt_i32_e32 vcc, v14, v7
	v_add_u32_e32 v4, 0x400, v2
	v_ashrrev_i32_e32 v5, 31, v4
	v_cndmask_b32_e32 v14, v6, v14, vcc
	v_lshlrev_b32_e32 v86, 2, v14
	v_xor_b32_e32 v14, 2, v6
	v_cmp_lt_i32_e32 vcc, v14, v7
	v_lshlrev_b32_e32 v93, 1, v4
	s_waitcnt vmcnt(17)
	v_add_u32_e32 v9, s58, v0
	v_cndmask_b32_e32 v14, v6, v14, vcc
	v_lshlrev_b32_e32 v87, 2, v14
	v_xor_b32_e32 v14, 1, v6
	v_cmp_lt_i32_e32 vcc, v14, v7
	v_ashrrev_i32_e32 v1, 1, v0
	s_lshl_b32 s6, s89, 11
	v_cndmask_b32_e32 v6, v6, v14, vcc
	v_lshlrev_b32_e32 v88, 2, v6
	v_lshlrev_b64 v[6:7], 2, v[4:5]
	v_add_u32_e32 v4, 0x500, v2
	v_ashrrev_i32_e32 v5, 31, v4
	v_lshl_add_u64 v[32:33], s[12:13], 0, v[6:7]
	v_lshl_add_u64 v[34:35], s[14:15], 0, v[6:7]
	v_lshlrev_b64 v[6:7], 2, v[4:5]
	v_lshlrev_b32_e32 v94, 1, v4
	v_add_u32_e32 v4, 0x600, v2
	v_ashrrev_i32_e32 v5, 31, v4
	v_lshl_add_u64 v[36:37], s[12:13], 0, v[6:7]
	v_lshl_add_u64 v[38:39], s[14:15], 0, v[6:7]
	v_lshlrev_b64 v[6:7], 2, v[4:5]
	v_lshlrev_b32_e32 v95, 1, v4
	v_add_u32_e32 v4, 0x700, v2
	v_and_b32_e32 v8, 15, v0
	v_and_b32_e32 v10, -8, v1
	s_add_i32 s6, s6, 0
	v_and_b32_e32 v1, 0x3fffffe0, v9
	v_ashrrev_i32_e32 v5, 31, v4
	v_lshl_add_u32 v11, v8, 7, s6
	v_and_b32_e32 v24, 0x7c, v2
	v_mov_b32_e32 v25, 0
	v_lshlrev_b32_e32 v1, 2, v1
	s_add_i32 s6, 0, 0x21000
	v_lshl_add_u64 v[40:41], s[12:13], 0, v[6:7]
	v_lshl_add_u64 v[42:43], s[14:15], 0, v[6:7]
	v_lshlrev_b64 v[6:7], 2, v[4:5]
	v_lshlrev_b32_e32 v96, 1, v4
	v_lshlrev_b32_e32 v4, 4, v9
	v_lshl_add_u64 v[26:27], s[18:19], 0, v[24:25]
	v_add3_u32 v81, 0, v1, v24
	v_add3_u32 v82, s6, v1, v24
	v_lshl_add_u64 v[44:45], s[12:13], 0, v[6:7]
	v_lshlrev_b32_e32 v24, 2, v8
	s_add_i32 s6, 0, 0x22000
	s_add_i32 s7, 0, 0x22200
	s_add_i32 s12, 0, 0x22400
	v_or_b32_e32 v5, 4, v4
	s_add_i32 s4, 0, 0x22600
	s_lshl_b32 s5, s89, 1
	v_lshl_add_u64 v[48:49], s[16:17], 0, v[24:25]
	v_add_u32_e32 v24, s6, v4
	v_add_u32_e32 v97, s7, v4
	v_add_u32_e32 v98, s12, v4
	v_add_u32_e32 v99, s6, v5
	v_add_u32_e32 v100, s7, v5
	v_add_u32_e32 v101, s12, v5
	v_or_b32_e32 v5, 8, v4
	v_or_b32_e32 v4, 12, v4
	v_add_u32_e32 v104, s12, v5
	v_add_u32_e32 v107, s12, v4
	s_add_u32 s12, s34, 0x4000
	s_addc_u32 s13, s35, 0
	v_lshl_add_u64 v[46:47], s[14:15], 0, v[6:7]
	s_add_u32 s14, s34, 0x186a0000
	s_addc_u32 s15, s35, 0
	s_add_u32 s16, s34, 0x187a0000
	v_add_u32_e32 v102, s6, v5
	v_add_u32_e32 v105, s6, v4
	s_addc_u32 s17, s35, 0
	s_lshl_b32 s6, s89, 9
	v_ashrrev_i32_e32 v1, 31, v0
	s_add_i32 s6, s6, 0
	v_cmp_eq_u32_e64 s[10:11], 0, v0
	v_and_b32_e32 v12, -16, v0
	v_lshlrev_b32_e32 v89, 3, v0
	v_add_u32_e32 v103, s7, v5
	v_add_u32_e32 v106, s7, v4
	v_lshl_add_u64 v[50:51], v[0:1], 3, s[38:39]
	s_movk_i32 s7, 0x1010
	v_mov_b32_e32 v0, s6
	v_lshlrev_b32_e32 v13, 7, v9
	v_mad_u32_u24 v0, v8, s7, v0
	s_mov_b32 s6, 0x10140
	v_add3_u32 v109, v0, v12, s6
	v_add_u32_e32 v0, 0, v13
	v_cmp_gt_i32_e64 s[8:9], 32, v9
	v_lshl_add_u32 v80, v9, 2, s4
	v_add_u32_e32 v90, 0x200, v89
	v_add_u32_e32 v91, 0x400, v89
	v_add_u32_e32 v92, 0x600, v89
	v_lshl_add_u64 v[52:53], v[2:3], 1, s[20:21]
	v_lshl_add_u32 v108, s89, 8, v10
	v_mov_b32_e32 v110, 0x3727c5ac
	s_mov_b32 s6, 0x800000
	s_movk_i32 s7, 0x80
	v_add_u32_e32 v111, v11, v12
	v_add_u32_e32 v112, 0x21000, v0
	v_mov_b32_e32 v113, 1
	v_mov_b32_e32 v114, 0xff61b1e6
	s_mov_b32 s28, s90
	global_load_dwordx4 v[172:175], v[28:29], off
	global_load_dwordx4 v[176:179], v[30:31], off
	global_load_dwordx4 v[180:183], v[28:29], off offset:1024
	global_load_dwordx4 v[184:187], v[30:31], off offset:1024
	global_load_dwordx4 v[188:191], v[28:29], off offset:2048
	global_load_dwordx4 v[192:195], v[30:31], off offset:2048
	global_load_dwordx4 v[200:203], v[28:29], off offset:3072
	global_load_dwordx4 v[204:207], v[30:31], off offset:3072
	global_load_dwordx4 v[208:211], v[32:33], off
	global_load_dwordx4 v[212:215], v[34:35], off
	global_load_dwordx4 v[216:219], v[36:37], off
	global_load_dwordx4 v[220:223], v[38:39], off
	global_load_dwordx4 v[224:227], v[40:41], off
	global_load_dwordx4 v[228:231], v[42:43], off
	global_load_dwordx4 v[232:235], v[44:45], off
	global_load_dwordx4 v[236:239], v[46:47], off
	s_branch .LBB0_438

; DI float bflo(unsigned w) { return __uint_as_float(w << 16); }
; DI float bfhi(unsigned w) { return __uint_as_float(w & 0xffff0000u); }
; DI void p4_ln_router(const Ctx& c) {
;     ...
;         for (int tt = 0; tt < 2; ++tt) { const int tl = 2 * w + tt, tok = tokbase + pass * 16 + tl;
;             const u32x2* src = (const u32x2*)(y1 + (size_t)tok * D); f32x4 v[8]; float s = 0.f;
; #pragma unroll
;             for (int i = 0; i < 8; ++i) { const u32x2 yv = src[i * 64 + lane]; v[i] = (f32x4){bflo(yv.x), bfhi(yv.x), bflo(yv.y), bfhi(yv.y)}; s += (v[i][0] + v[i][1]) + (v[i][2] + v[i][3]); }
; #pragma unroll
;             for (int o = 32; o >= 1; o >>= 1) s += __shfl_xor(s, o);
;             const float mean = s * (1.0f / D); float qv = 0.f;
; #pragma unroll
;             for (int i = 0; i < 8; ++i) { const f32x4 dl = v[i] - mean; qv += (dl[0] * dl[0] + dl[1] * dl[1]) + (dl[2] * dl[2] + dl[3] * dl[3]); }
; #pragma unroll
;             for (int o = 32; o >= 1; o >>= 1) qv += __shfl_xor(qv, o);
;             const float rstd = rsqrtf(qv * (1.0f / D) + LN_EPS);
;             if (lane == 0) { st1[2 * tok] = mean; st1[2 * tok + 1] = rstd; }
; #pragma unroll
;             for (int i = 0; i < 8; ++i) { const int d = (i * 64 + lane) * 4; const f32x4 g = *(const f32x4*)(lw + d), bb = *(const f32x4*)(lb + d);
.LBB0_442:
	s_or_b64 exec, exec, s[26:27]
	v_mov_b32_e32 v68, v62
	v_mov_b32_e32 v69, v60
	v_mov_b32_e32 v72, v66
	v_mov_b32_e32 v73, v64
	v_pk_mul_f32 v[72:73], v[72:73], v[4:5] op_sel_hi:[1,0]
	v_pk_mul_f32 v[120:121], v[68:69], v[4:5] op_sel_hi:[1,0]
	s_lshl_b64 s[24:25], s[24:25], 11
	v_lshl_add_u64 v[68:69], s[24:25], 1, v[52:53]
	v_mov_b32_e32 v60, v63
	v_mov_b32_e32 v64, v67
	v_pk_mul_f32 v[62:63], v[64:65], v[4:5] op_sel_hi:[1,0]
	v_pk_mul_f32 v[64:65], v[60:61], v[4:5] op_sel_hi:[1,0]
	v_mov_b32_e32 v57, v58
	v_pk_mul_f32 v[58:59], v[78:79], v[4:5] op_sel_hi:[1,0]
	v_pk_mul_f32 v[56:57], v[56:57], v[4:5] op_sel_hi:[1,0]
	v_pk_mul_f32 v[54:55], v[54:55], v[4:5] op_sel_hi:[1,0]
	v_pk_mul_f32 v[22:23], v[22:23], v[4:5] op_sel_hi:[1,0]
	v_mov_b32_e32 v14, v19
	v_mov_b32_e32 v16, v21
	v_pk_mul_f32 v[16:17], v[16:17], v[4:5] op_sel_hi:[1,0]
	v_pk_mul_f32 v[14:15], v[14:15], v[4:5] op_sel_hi:[1,0]
	v_mov_b32_e32 v11, v12
	v_pk_mul_f32 v[12:13], v[70:71], v[4:5] op_sel_hi:[1,0]
	v_pk_mul_f32 v[10:11], v[10:11], v[4:5] op_sel_hi:[1,0]
	v_pk_mul_f32 v[8:9], v[8:9], v[4:5] op_sel_hi:[1,0]
	v_pk_mul_f32 v[6:7], v[6:7], v[4:5] op_sel_hi:[1,0]
	v_mov_b32_e32 v0, v5
	v_pk_mul_f32 v[124:125], v[0:1], v[4:5] op_sel_hi:[1,0]
	s_mul_i32 s25, s36, 0x1010
	s_xor_b64 s[26:27], s[22:23], -1
	s_add_i32 s25, s25, 0
	s_and_b64 vcc, exec, s[26:27]
	s_add_i32 s26, s25, 0x10100
	v_add_u32_e32 v115, s25, v89
	v_add_u32_e32 v133, s26, v89
	v_add_u32_e32 v126, s25, v90
	v_add_u32_e32 v134, s26, v90
	v_add_u32_e32 v127, s25, v91
	v_add_u32_e32 v135, s26, v91
	v_add_u32_e32 v128, s25, v92
	v_add_u32_e32 v136, s26, v92
	v_add_u32_e32 v129, s25, v93
	v_add_u32_e32 v137, s26, v93
	v_add_u32_e32 v130, s25, v94
	v_add_u32_e32 v138, s26, v94
	v_add_u32_e32 v131, s25, v95
	v_add_u32_e32 v139, s26, v95
	s_mov_b32 s24, 1
	s_mov_b64 s[22:23], 0
	v_add_u32_e32 v132, s25, v96
	v_add_u32_e32 v140, s26, v96
	s_waitcnt vmcnt(0)
; DI float bflo(unsigned w) { return __uint_as_float(w << 16); }
; DI float bfhi(unsigned w) { return __uint_as_float(w & 0xffff0000u); }
; DI u32x2 pack4(f32x4 v) { bf16x4_t r = __builtin_convertvector(v, bf16x4_t); return __builtin_bit_cast(u32x2, r); }
; DI void p4_ln_router(const Ctx& c) {
;     ...
;             for (int i = 0; i < 8; ++i) { const int d = (i * 64 + lane) * 4; const f32x4 g = *(const f32x4*)(lw + d), bb = *(const f32x4*)(lb + d);
;                 const f32x4 xv = (v[i] - mean) * rstd * g + bb;
;                 const u32x2 hi = pack4(xv); const f32x4 rsd = {xv[0] - bflo(hi.x), xv[1] - bfhi(hi.x), xv[2] - bflo(hi.y), xv[3] - bfhi(hi.y)};
;                 *(u32x2*)(x1b + (size_t)tok * D + d) = hi;
;                 *LP(u32x2, Xhi + tl * XSTR + d * 2) = hi; *LP(u32x2, Xlo + tl * XSTR + d * 2) = pack4(rsd); } }
	v_pk_fma_f32 v[72:73], v[72:73], v[174:175], v[178:179]
	v_pk_fma_f32 v[74:75], v[120:121], v[172:173], v[176:177]
	v_cvt_pk_bf16_f32 v77, v72, v73
	v_cvt_pk_bf16_f32 v76, v74, v75
	global_store_dwordx2 v[68:69], v[76:77], off
	v_pk_fma_f32 v[60:61], v[62:63], v[182:183], v[186:187]
	v_pk_fma_f32 v[62:63], v[64:65], v[180:181], v[184:185]
	v_cvt_pk_bf16_f32 v65, v60, v61
	v_cvt_pk_bf16_f32 v64, v62, v63
	global_store_dwordx2 v[68:69], v[64:65], off offset:512
	v_pk_fma_f32 v[66:67], v[58:59], v[190:191], v[194:195]
	v_pk_fma_f32 v[78:79], v[56:57], v[188:189], v[192:193]
	v_cvt_pk_bf16_f32 v121, v66, v67
	v_cvt_pk_bf16_f32 v120, v78, v79
	global_store_dwordx2 v[68:69], v[120:121], off offset:1024
	v_pk_fma_f32 v[58:59], v[54:55], v[202:203], v[206:207]
	v_pk_fma_f32 v[22:23], v[22:23], v[200:201], v[204:205]
	v_cvt_pk_bf16_f32 v123, v58, v59
	v_cvt_pk_bf16_f32 v122, v22, v23
	global_store_dwordx2 v[68:69], v[122:123], off offset:1536
	v_pk_fma_f32 v[56:57], v[16:17], v[210:211], v[214:215]
	v_pk_fma_f32 v[54:55], v[14:15], v[208:209], v[212:213]
	v_cvt_pk_bf16_f32 v117, v56, v57
	v_cvt_pk_bf16_f32 v116, v54, v55
	global_store_dwordx2 v[68:69], v[116:117], off offset:2048
	v_pk_mul_f32 v[118:119], v[2:3], v[4:5] op_sel_hi:[1,0]
	v_pk_fma_f32 v[20:21], v[12:13], v[218:219], v[222:223]
	v_pk_fma_f32 v[18:19], v[10:11], v[216:217], v[220:221]
	v_cvt_pk_bf16_f32 v71, v20, v21
	v_cvt_pk_bf16_f32 v70, v18, v19
	global_store_dwordx2 v[68:69], v[70:71], off offset:2560
	v_pk_fma_f32 v[8:9], v[8:9], v[226:227], v[230:231]
	v_pk_fma_f32 v[10:11], v[6:7], v[224:225], v[228:229]
	v_cvt_pk_bf16_f32 v13, v8, v9
	v_cvt_pk_bf16_f32 v12, v10, v11
	global_store_dwordx2 v[68:69], v[12:13], off offset:3072
	v_lshlrev_b32_e32 v14, 16, v76
	v_and_b32_e32 v15, 0xffff0000, v76
	v_lshlrev_b32_e32 v16, 16, v77
	v_and_b32_e32 v17, 0xffff0000, v77
	v_pk_add_f32 v[14:15], v[74:75], v[14:15] neg_lo:[0,1] neg_hi:[0,1]
	v_pk_add_f32 v[16:17], v[72:73], v[16:17] neg_lo:[0,1] neg_hi:[0,1]
	ds_write_b64 v115, v[76:77]
	v_cvt_pk_bf16_f32 v17, v16, v17
	v_cvt_pk_bf16_f32 v16, v14, v15
	ds_write_b64 v133, v[16:17]
	v_lshlrev_b32_e32 v14, 16, v64
	v_and_b32_e32 v15, 0xffff0000, v64
	v_lshlrev_b32_e32 v16, 16, v65
	v_and_b32_e32 v17, 0xffff0000, v65
	v_pk_add_f32 v[14:15], v[62:63], v[14:15] neg_lo:[0,1] neg_hi:[0,1]
	v_pk_add_f32 v[16:17], v[60:61], v[16:17] neg_lo:[0,1] neg_hi:[0,1]
	ds_write_b64 v126, v[64:65]
	v_cvt_pk_bf16_f32 v17, v16, v17
	v_cvt_pk_bf16_f32 v16, v14, v15
	ds_write_b64 v134, v[16:17]
	v_lshlrev_b32_e32 v14, 16, v120
	v_and_b32_e32 v15, 0xffff0000, v120
	v_lshlrev_b32_e32 v16, 16, v121
	v_and_b32_e32 v17, 0xffff0000, v121
	v_pk_add_f32 v[14:15], v[78:79], v[14:15] neg_lo:[0,1] neg_hi:[0,1]
	v_pk_add_f32 v[16:17], v[66:67], v[16:17] neg_lo:[0,1] neg_hi:[0,1]
	ds_write_b64 v127, v[120:121]
	v_cvt_pk_bf16_f32 v17, v16, v17
	v_cvt_pk_bf16_f32 v16, v14, v15
	ds_write_b64 v135, v[16:17]
	v_lshlrev_b32_e32 v14, 16, v122
	v_and_b32_e32 v15, 0xffff0000, v122
	v_lshlrev_b32_e32 v16, 16, v123
	v_and_b32_e32 v17, 0xffff0000, v123
	v_pk_add_f32 v[14:15], v[22:23], v[14:15] neg_lo:[0,1] neg_hi:[0,1]
	v_pk_add_f32 v[16:17], v[58:59], v[16:17] neg_lo:[0,1] neg_hi:[0,1]
	ds_write_b64 v128, v[122:123]
	v_cvt_pk_bf16_f32 v17, v16, v17
	v_cvt_pk_bf16_f32 v16, v14, v15
	ds_write_b64 v136, v[16:17]
	v_lshlrev_b32_e32 v14, 16, v116
	v_and_b32_e32 v15, 0xffff0000, v116
	v_lshlrev_b32_e32 v16, 16, v117
	v_and_b32_e32 v17, 0xffff0000, v117
	v_pk_add_f32 v[14:15], v[54:55], v[14:15] neg_lo:[0,1] neg_hi:[0,1]
	v_pk_add_f32 v[16:17], v[56:57], v[16:17] neg_lo:[0,1] neg_hi:[0,1]
	ds_write_b64 v129, v[116:117]
	v_cvt_pk_bf16_f32 v17, v16, v17
	v_cvt_pk_bf16_f32 v16, v14, v15
	ds_write_b64 v137, v[16:17]
	v_lshlrev_b32_e32 v14, 16, v70
	v_and_b32_e32 v15, 0xffff0000, v70
	v_lshlrev_b32_e32 v16, 16, v71
	v_and_b32_e32 v17, 0xffff0000, v71
	v_pk_add_f32 v[14:15], v[18:19], v[14:15] neg_lo:[0,1] neg_hi:[0,1]
	v_pk_add_f32 v[16:17], v[20:21], v[16:17] neg_lo:[0,1] neg_hi:[0,1]
	ds_write_b64 v130, v[70:71]
	v_cvt_pk_bf16_f32 v17, v16, v17
	v_cvt_pk_bf16_f32 v16, v14, v15
	ds_write_b64 v138, v[16:17]
	v_lshlrev_b32_e32 v14, 16, v12
	v_and_b32_e32 v15, 0xffff0000, v12
	v_lshlrev_b32_e32 v16, 16, v13
	v_and_b32_e32 v17, 0xffff0000, v13
	v_pk_add_f32 v[10:11], v[10:11], v[14:15] neg_lo:[0,1] neg_hi:[0,1]
	v_pk_add_f32 v[8:9], v[8:9], v[16:17] neg_lo:[0,1] neg_hi:[0,1]
	ds_write_b64 v131, v[12:13]
	v_cvt_pk_bf16_f32 v9, v8, v9
	v_cvt_pk_bf16_f32 v8, v10, v11
	ds_write_b64 v139, v[8:9]
	v_pk_fma_f32 v[2:3], v[124:125], v[234:235], v[238:239]
	v_pk_fma_f32 v[0:1], v[118:119], v[232:233], v[236:237]
	v_cvt_pk_bf16_f32 v5, v2, v3
	v_cvt_pk_bf16_f32 v4, v0, v1
	v_lshlrev_b32_e32 v6, 16, v4
	v_and_b32_e32 v7, 0xffff0000, v4
	v_lshlrev_b32_e32 v8, 16, v5
	v_and_b32_e32 v9, 0xffff0000, v5
	v_pk_add_f32 v[0:1], v[0:1], v[6:7] neg_lo:[0,1] neg_hi:[0,1]
	v_pk_add_f32 v[2:3], v[2:3], v[8:9] neg_lo:[0,1] neg_hi:[0,1]
	global_store_dwordx2 v[68:69], v[4:5], off offset:3584
	v_cvt_pk_bf16_f32 v3, v2, v3
	v_cvt_pk_bf16_f32 v2, v0, v1
	ds_write_b64 v132, v[4:5]
	ds_write_b64 v140, v[2:3]
	s_cbranch_vccnz .LBB0_445
